# baseline (speedup 1.0000x reference)
.Lq_go_2:
	ds_read_b128 v[228:231], v5 offset:32768
	ds_read_b128 v[232:235], v5 offset:33280
	ds_read_b128 v[236:239], v5 offset:33792
	ds_read_b128 v[240:243], v5 offset:34304
	v_mul_f32_e32 v244, v148, v152
	v_mul_f32_e32 v250, v149, v153
	v_mul_f32_e64 v245, -v152, v152
	v_mul_f32_e64 v251, -v153, v153
	v_add_f32_e32 v246, v148, v152
	v_add_f32_e32 v252, v149, v153
	v_fma_f32 v245, -v148, v148, v245
	v_fma_f32 v251, -v149, v149, v251
	v_fma_f32 v247, v10, v246, v11
	v_fma_f32 v253, v10, v252, v11
	v_fma_f32 v246, v13, v160, v14
	v_fma_f32 v252, v13, v161, v14
	v_fma_f32 v248, v12, v156, v245
	v_fma_f32 v254, v12, v157, v251
	v_fma_f32 v249, 2.0, v244, v247
	v_fma_f32 v255, 2.0, v250, v253
	v_sub_f32_e32 v247, v247, v245
	v_sub_f32_e32 v253, v253, v251
	v_fma_f32 v246, -2.0, v244, v246
	v_fma_f32 v252, -2.0, v250, v252
	v_mul_f32_e32 v247, v247, v248
	v_mul_f32_e32 v253, v253, v254
	v_rcp_f32_e32 v247, v247
	v_rcp_f32_e32 v253, v253
	v_mul_f32_e32 v249, v249, v246
	v_mul_f32_e32 v255, v255, v252
	v_fma_f32 v19, v249, v247, v19
	v_fma_f32 v19, v255, v253, v19
	v_mul_f32_e32 v244, v150, v154
	v_mul_f32_e32 v250, v151, v155
	v_mul_f32_e64 v245, -v154, v154
	v_mul_f32_e64 v251, -v155, v155
	v_add_f32_e32 v246, v150, v154
	v_add_f32_e32 v252, v151, v155
	v_fma_f32 v245, -v150, v150, v245
	v_fma_f32 v251, -v151, v151, v251
	v_fma_f32 v247, v10, v246, v11
	v_fma_f32 v253, v10, v252, v11
	v_fma_f32 v246, v13, v162, v14
	v_fma_f32 v252, v13, v163, v14
	v_fma_f32 v248, v12, v158, v245
	v_fma_f32 v254, v12, v159, v251
	v_fma_f32 v249, 2.0, v244, v247
	v_fma_f32 v255, 2.0, v250, v253
	v_sub_f32_e32 v247, v247, v245
	v_sub_f32_e32 v253, v253, v251
	v_fma_f32 v246, -2.0, v244, v246
	v_fma_f32 v252, -2.0, v250, v252
	v_mul_f32_e32 v247, v247, v248
	v_mul_f32_e32 v253, v253, v254
	v_rcp_f32_e32 v247, v247
	v_rcp_f32_e32 v253, v253
	v_mul_f32_e32 v249, v249, v246
	v_mul_f32_e32 v255, v255, v252
	v_fma_f32 v20, v249, v247, v20
	v_fma_f32 v20, v255, v253, v20
	s_waitcnt lgkmcnt(0)
	v_mfma_f32_16x16x32_f16 v[148:151], v[28:31], v[228:231], 0
	v_mfma_f32_16x16x32_f16 v[152:155], v[28:31], v[232:235], 0
	v_mfma_f32_16x16x32_f16 v[156:159], v[28:31], v[236:239], v[0:3]
	v_mfma_f32_16x16x32_f16 v[160:163], v[28:31], v[240:243], 0
	v_mfma_f32_16x16x32_f16 v[148:151], v[32:35], v[100:103], v[148:151]
	v_mfma_f32_16x16x32_f16 v[152:155], v[32:35], v[108:111], v[152:155]
	v_mfma_f32_16x16x32_f16 v[156:159], v[32:35], v[116:119], v[156:159]
	v_mfma_f32_16x16x32_f16 v[160:163], v[32:35], v[124:127], v[160:163]
	v_mul_f32_e32 v244, v132, v136
	v_mul_f32_e32 v250, v133, v137
	v_mul_f32_e64 v245, -v136, v136
	v_mul_f32_e64 v251, -v137, v137
	v_add_f32_e32 v246, v132, v136
	v_add_f32_e32 v252, v133, v137
	v_fma_f32 v245, -v132, v132, v245
	v_fma_f32 v251, -v133, v133, v251
	v_fma_f32 v247, v10, v246, v11
	v_fma_f32 v253, v10, v252, v11
	v_fma_f32 v246, v13, v144, v14
	v_fma_f32 v252, v13, v145, v14
	v_fma_f32 v248, v12, v140, v245
	v_fma_f32 v254, v12, v141, v251
	v_fma_f32 v249, 2.0, v244, v247
	v_fma_f32 v255, 2.0, v250, v253
	v_sub_f32_e32 v247, v247, v245
	v_sub_f32_e32 v253, v253, v251
	v_fma_f32 v246, -2.0, v244, v246
	v_fma_f32 v252, -2.0, v250, v252
	v_mul_f32_e32 v247, v247, v248
	v_mul_f32_e32 v253, v253, v254
	v_rcp_f32_e32 v247, v247
	v_rcp_f32_e32 v253, v253
	v_mul_f32_e32 v249, v249, v246
	v_mul_f32_e32 v255, v255, v252
	v_fma_f32 v19, v249, v247, v19
	v_fma_f32 v19, v255, v253, v19
	v_mul_f32_e32 v244, v134, v138
	v_mul_f32_e32 v250, v135, v139
	v_mul_f32_e64 v245, -v138, v138
	v_mul_f32_e64 v251, -v139, v139
	v_add_f32_e32 v246, v134, v138
	v_add_f32_e32 v252, v135, v139
	v_fma_f32 v245, -v134, v134, v245
	v_fma_f32 v251, -v135, v135, v251
	v_fma_f32 v247, v10, v246, v11
	v_fma_f32 v253, v10, v252, v11
	v_fma_f32 v246, v13, v146, v14
	v_fma_f32 v252, v13, v147, v14
	v_fma_f32 v248, v12, v142, v245
	v_fma_f32 v254, v12, v143, v251
	v_fma_f32 v249, 2.0, v244, v247
	v_fma_f32 v255, 2.0, v250, v253
	v_sub_f32_e32 v247, v247, v245
	v_sub_f32_e32 v253, v253, v251
	v_fma_f32 v246, -2.0, v244, v246
	v_fma_f32 v252, -2.0, v250, v252
	v_mul_f32_e32 v247, v247, v248
	v_mul_f32_e32 v253, v253, v254
	v_rcp_f32_e32 v247, v247
	v_rcp_f32_e32 v253, v253
	v_mul_f32_e32 v249, v249, v246
	v_mul_f32_e32 v255, v255, v252
	v_fma_f32 v20, v249, v247, v20
	v_fma_f32 v20, v255, v253, v20
	v_mul_f32_e32 v244, v148, v152
	v_mul_f32_e32 v250, v149, v153
	v_mul_f32_e64 v245, -v152, v152
	v_mul_f32_e64 v251, -v153, v153
	v_add_f32_e32 v246, v148, v152
	v_add_f32_e32 v252, v149, v153
	v_fma_f32 v245, -v148, v148, v245
	v_fma_f32 v251, -v149, v149, v251
	v_fma_f32 v247, v10, v246, v11
	v_fma_f32 v253, v10, v252, v11
	v_fma_f32 v246, v13, v160, v14
	v_fma_f32 v252, v13, v161, v14
	v_fma_f32 v248, v12, v156, v245
	v_fma_f32 v254, v12, v157, v251
	v_fma_f32 v249, 2.0, v244, v247
	v_fma_f32 v255, 2.0, v250, v253
	v_sub_f32_e32 v247, v247, v245
	v_sub_f32_e32 v253, v253, v251
	v_fma_f32 v246, -2.0, v244, v246
	v_fma_f32 v252, -2.0, v250, v252
	v_mul_f32_e32 v247, v247, v248
	v_mul_f32_e32 v253, v253, v254
	v_rcp_f32_e32 v247, v247
	v_rcp_f32_e32 v253, v253
	v_mul_f32_e32 v249, v249, v246
	v_mul_f32_e32 v255, v255, v252
	v_mul_f32_e32 v249, v249, v247
	v_mul_f32_e32 v255, v255, v253
	v_fma_f32 v19, v249, v15, v19
	v_fma_f32 v19, v255, v16, v19
	v_mul_f32_e32 v244, v150, v154
	v_mul_f32_e32 v250, v151, v155
	v_mul_f32_e64 v245, -v154, v154
	v_mul_f32_e64 v251, -v155, v155
	v_add_f32_e32 v246, v150, v154
	v_add_f32_e32 v252, v151, v155
	v_fma_f32 v245, -v150, v150, v245
	v_fma_f32 v251, -v151, v151, v251
	v_fma_f32 v247, v10, v246, v11
	v_fma_f32 v253, v10, v252, v11
	v_fma_f32 v246, v13, v162, v14
	v_fma_f32 v252, v13, v163, v14
	v_fma_f32 v248, v12, v158, v245
	v_fma_f32 v254, v12, v159, v251
	v_fma_f32 v249, 2.0, v244, v247
	v_fma_f32 v255, 2.0, v250, v253
	v_sub_f32_e32 v247, v247, v245
	v_sub_f32_e32 v253, v253, v251
	v_fma_f32 v246, -2.0, v244, v246
	v_fma_f32 v252, -2.0, v250, v252
	v_mul_f32_e32 v247, v247, v248
	v_mul_f32_e32 v253, v253, v254
	v_rcp_f32_e32 v247, v247
	v_rcp_f32_e32 v253, v253
	v_mul_f32_e32 v249, v249, v246
	v_mul_f32_e32 v255, v255, v252
	v_mul_f32_e32 v249, v249, v247
	v_mul_f32_e32 v255, v255, v253
	v_fma_f32 v20, v249, v17, v20
	v_fma_f32 v20, v255, v18, v20
	v_xor_b32_e32 v23, 32, v8
	v_lshlrev_b32_e32 v23, 2, v23
	s_waitcnt vmcnt(4)
	v_cvt_pk_f16_f32 v100, v164, v168
	v_cvt_pk_f16_f32 v116, v180, v184
	v_pk_add_f16 v100, v100, -0.5 op_sel_hi:[1,0]
	v_pk_add_f16 v116, v116, -0.5 op_sel_hi:[1,0]
	v_pk_mul_f16 v132, v116, v116
	v_pk_mul_f16 v148, v100, v116
	v_pk_fma_f16 v132, v100, v100, v132
	v_cvt_pk_f16_f32 v104, v165, v169
	v_cvt_pk_f16_f32 v120, v181, v185
	v_pk_add_f16 v104, v104, -0.5 op_sel_hi:[1,0]
	v_pk_add_f16 v120, v120, -0.5 op_sel_hi:[1,0]
	v_pk_mul_f16 v136, v120, v120
	v_pk_mul_f16 v152, v104, v120
	v_pk_fma_f16 v136, v104, v104, v136
	v_cvt_pk_f16_f32 v108, v166, v170
	v_cvt_pk_f16_f32 v124, v182, v186
	v_pk_add_f16 v108, v108, -0.5 op_sel_hi:[1,0]
	v_pk_add_f16 v124, v124, -0.5 op_sel_hi:[1,0]
	v_pk_mul_f16 v140, v124, v124
	v_pk_mul_f16 v156, v108, v124
	v_pk_fma_f16 v140, v108, v108, v140
	v_cvt_pk_f16_f32 v112, v167, v171
	v_cvt_pk_f16_f32 v128, v183, v187
	v_pk_add_f16 v112, v112, -0.5 op_sel_hi:[1,0]
	v_pk_add_f16 v128, v128, -0.5 op_sel_hi:[1,0]
	v_pk_mul_f16 v144, v128, v128
	v_pk_mul_f16 v160, v112, v128
	v_pk_fma_f16 v144, v112, v112, v144
	ds_bpermute_b32 v102, v23, v100
	ds_bpermute_b32 v106, v23, v104
	ds_bpermute_b32 v110, v23, v108
	ds_bpermute_b32 v114, v23, v112
	ds_bpermute_b32 v118, v23, v116
	ds_bpermute_b32 v122, v23, v120
	ds_bpermute_b32 v126, v23, v124
	ds_bpermute_b32 v130, v23, v128
	s_waitcnt vmcnt(0)
	v_cvt_pk_f16_f32 v101, v172, v176
	v_cvt_pk_f16_f32 v117, v188, v192
	v_pk_add_f16 v101, v101, -0.5 op_sel_hi:[1,0]
	v_pk_add_f16 v117, v117, -0.5 op_sel_hi:[1,0]
	v_pk_mul_f16 v133, v117, v117
	v_pk_mul_f16 v149, v101, v117
	v_pk_fma_f16 v133, v101, v101, v133
	v_cvt_pk_f16_f32 v105, v173, v177
	v_cvt_pk_f16_f32 v121, v189, v193
	v_pk_add_f16 v105, v105, -0.5 op_sel_hi:[1,0]
	v_pk_add_f16 v121, v121, -0.5 op_sel_hi:[1,0]
	v_pk_mul_f16 v137, v121, v121
	v_pk_mul_f16 v153, v105, v121
	v_pk_fma_f16 v137, v105, v105, v137
	v_cvt_pk_f16_f32 v109, v174, v178
	v_cvt_pk_f16_f32 v125, v190, v194
	v_pk_add_f16 v109, v109, -0.5 op_sel_hi:[1,0]
	v_pk_add_f16 v125, v125, -0.5 op_sel_hi:[1,0]
	v_pk_mul_f16 v141, v125, v125
	v_pk_mul_f16 v157, v109, v125
	v_pk_fma_f16 v141, v109, v109, v141
	v_cvt_pk_f16_f32 v113, v175, v179
	v_cvt_pk_f16_f32 v129, v191, v195
	v_pk_add_f16 v113, v113, -0.5 op_sel_hi:[1,0]
	v_pk_add_f16 v129, v129, -0.5 op_sel_hi:[1,0]
	v_pk_mul_f16 v145, v129, v129
	v_pk_mul_f16 v161, v113, v129
	v_pk_fma_f16 v145, v113, v113, v145
	s_waitcnt lgkmcnt(7)
	ds_bpermute_b32 v134, v23, v132
	ds_bpermute_b32 v138, v23, v136
	ds_bpermute_b32 v142, v23, v140
	ds_bpermute_b32 v146, v23, v144
	ds_bpermute_b32 v150, v23, v148
	ds_bpermute_b32 v154, v23, v152
	ds_bpermute_b32 v158, v23, v156
	ds_bpermute_b32 v162, v23, v160
	s_waitcnt lgkmcnt(7)
	ds_bpermute_b32 v103, v23, v101
	ds_bpermute_b32 v107, v23, v105
	ds_bpermute_b32 v111, v23, v109
	ds_bpermute_b32 v115, v23, v113
	ds_bpermute_b32 v119, v23, v117
	ds_bpermute_b32 v123, v23, v121
	ds_bpermute_b32 v127, v23, v125
	ds_bpermute_b32 v131, v23, v129
	s_waitcnt lgkmcnt(7)
	ds_bpermute_b32 v135, v23, v133
	ds_bpermute_b32 v139, v23, v137
	ds_bpermute_b32 v143, v23, v141
	ds_bpermute_b32 v147, v23, v145
	ds_bpermute_b32 v151, v23, v149
	ds_bpermute_b32 v155, v23, v153
	ds_bpermute_b32 v159, v23, v157
	ds_bpermute_b32 v163, v23, v161
	s_waitcnt lgkmcnt(0)
	v_mfma_f32_16x16x32_f16 v[196:199], v[36:39], v[28:31], 0
	v_mfma_f32_16x16x32_f16 v[200:203], v[40:43], v[28:31], 0
	v_mfma_f32_16x16x32_f16 v[204:207], v[44:47], v[28:31], 0
	v_mfma_f32_16x16x32_f16 v[208:211], v[48:51], v[28:31], 0
	v_mfma_f32_16x16x32_f16 v[196:199], v[100:103], v[32:35], v[196:199]
	v_mfma_f32_16x16x32_f16 v[200:203], v[104:107], v[32:35], v[200:203]
	v_mfma_f32_16x16x32_f16 v[204:207], v[108:111], v[32:35], v[204:207]
	v_mfma_f32_16x16x32_f16 v[208:211], v[112:115], v[32:35], v[208:211]
	v_mfma_f32_16x16x32_f16 v[212:215], v[52:55], v[28:31], 0
	v_mfma_f32_16x16x32_f16 v[216:219], v[56:59], v[28:31], 0
	v_mfma_f32_16x16x32_f16 v[220:223], v[60:63], v[28:31], 0
	v_mfma_f32_16x16x32_f16 v[224:227], v[64:67], v[28:31], 0
	v_mfma_f32_16x16x32_f16 v[212:215], v[116:119], v[32:35], v[212:215]
	v_mfma_f32_16x16x32_f16 v[216:219], v[120:123], v[32:35], v[216:219]
	v_mfma_f32_16x16x32_f16 v[220:223], v[124:127], v[32:35], v[220:223]
	v_mfma_f32_16x16x32_f16 v[224:227], v[128:131], v[32:35], v[224:227]
	v_cvt_pk_f16_f32 v164, v196, v200
	v_cvt_pk_f16_f32 v165, v204, v208
	v_cvt_pk_f16_f32 v166, v197, v201
	v_cvt_pk_f16_f32 v167, v205, v209
	v_cvt_pk_f16_f32 v168, v198, v202
	v_cvt_pk_f16_f32 v169, v206, v210
	v_cvt_pk_f16_f32 v170, v199, v203
	v_cvt_pk_f16_f32 v171, v207, v211
	v_mfma_f32_16x16x32_f16 v[196:199], v[68:71], v[28:31], 0
	v_mfma_f32_16x16x32_f16 v[200:203], v[72:75], v[28:31], 0
	v_mfma_f32_16x16x32_f16 v[204:207], v[76:79], v[28:31], 0
	v_mfma_f32_16x16x32_f16 v[208:211], v[80:83], v[28:31], 0
	v_mfma_f32_16x16x32_f16 v[196:199], v[132:135], v[32:35], v[196:199]
	v_mfma_f32_16x16x32_f16 v[200:203], v[136:139], v[32:35], v[200:203]
	v_mfma_f32_16x16x32_f16 v[204:207], v[140:143], v[32:35], v[204:207]
	v_mfma_f32_16x16x32_f16 v[208:211], v[144:147], v[32:35], v[208:211]
	v_cvt_pk_f16_f32 v172, v212, v216
	v_cvt_pk_f16_f32 v173, v220, v224
	v_cvt_pk_f16_f32 v174, v213, v217
	v_cvt_pk_f16_f32 v175, v221, v225
	v_cvt_pk_f16_f32 v176, v214, v218
	v_cvt_pk_f16_f32 v177, v222, v226
	v_cvt_pk_f16_f32 v178, v215, v219
	v_cvt_pk_f16_f32 v179, v223, v227
	v_mfma_f32_16x16x32_f16 v[212:215], v[84:87], v[28:31], 0
	v_mfma_f32_16x16x32_f16 v[216:219], v[88:91], v[28:31], 0
	v_mfma_f32_16x16x32_f16 v[220:223], v[92:95], v[28:31], 0
	v_mfma_f32_16x16x32_f16 v[224:227], v[96:99], v[28:31], 0
	v_mfma_f32_16x16x32_f16 v[212:215], v[148:151], v[32:35], v[212:215]
	v_mfma_f32_16x16x32_f16 v[216:219], v[152:155], v[32:35], v[216:219]
	v_mfma_f32_16x16x32_f16 v[220:223], v[156:159], v[32:35], v[220:223]
	v_mfma_f32_16x16x32_f16 v[224:227], v[160:163], v[32:35], v[224:227]
	v_cvt_pk_f16_f32 v180, v196, v200
	v_cvt_pk_f16_f32 v181, v204, v208
	v_cvt_pk_f16_f32 v182, v197, v201
	v_cvt_pk_f16_f32 v183, v205, v209
	v_cvt_pk_f16_f32 v184, v198, v202
	v_cvt_pk_f16_f32 v185, v206, v210
	v_cvt_pk_f16_f32 v186, v199, v203
	v_cvt_pk_f16_f32 v187, v207, v211
	v_cvt_pk_f16_f32 v188, v212, v216
	v_cvt_pk_f16_f32 v189, v220, v224
	v_cvt_pk_f16_f32 v190, v213, v217
	v_cvt_pk_f16_f32 v191, v221, v225
	v_cvt_pk_f16_f32 v192, v214, v218
	v_cvt_pk_f16_f32 v193, v222, v226
	v_cvt_pk_f16_f32 v194, v215, v219
	v_cvt_pk_f16_f32 v195, v223, v227
	s_mov_b64 exec, s[38:39]
	ds_write_b128 v4, v[168:171] offset:49152
	ds_write_b128 v4, v[176:179] offset:49664
	ds_write_b128 v4, v[184:187] offset:50176
	ds_write_b128 v4, v[192:195] offset:50688
	s_mov_b64 exec, -1
	v_mfma_f32_16x16x32_f16 v[196:199], v[24:27], v[164:167], 0
	v_mfma_f32_16x16x32_f16 v[200:203], v[24:27], v[172:175], 0
	v_mfma_f32_16x16x32_f16 v[204:207], v[24:27], v[180:183], v[0:3]
	v_mfma_f32_16x16x32_f16 v[208:211], v[24:27], v[188:191], 0
	v_mfma_f32_16x16x32_f16 v[212:215], v[28:31], v[164:167], 0
	v_mfma_f32_16x16x32_f16 v[216:219], v[28:31], v[172:175], 0
	v_mfma_f32_16x16x32_f16 v[220:223], v[28:31], v[180:183], v[0:3]
	v_mfma_f32_16x16x32_f16 v[224:227], v[28:31], v[188:191], 0
	v_mfma_f32_16x16x32_f16 v[212:215], v[32:35], v[168:171], v[212:215]
	v_mfma_f32_16x16x32_f16 v[216:219], v[32:35], v[176:179], v[216:219]
	v_mfma_f32_16x16x32_f16 v[220:223], v[32:35], v[184:187], v[220:223]
	v_mfma_f32_16x16x32_f16 v[224:227], v[32:35], v[192:195], v[224:227]
	s_waitcnt lgkmcnt(0)
	ds_write_b32 v6, v6 offset:96
	ds_read_b32 v9, v7 offset:96
	v_mul_f32_e32 v244, v196, v200
	v_mul_f32_e32 v250, v197, v201
	v_mul_f32_e64 v245, -v200, v200
	v_mul_f32_e64 v251, -v201, v201
	v_add_f32_e32 v246, v196, v200
	v_add_f32_e32 v252, v197, v201
	v_fma_f32 v245, -v196, v196, v245
	v_fma_f32 v251, -v197, v197, v251
	v_fma_f32 v247, v10, v246, v11
	v_fma_f32 v253, v10, v252, v11
	v_fma_f32 v246, v13, v208, v14
	v_fma_f32 v252, v13, v209, v14
	v_fma_f32 v248, v12, v204, v245
	v_fma_f32 v254, v12, v205, v251
	v_fma_f32 v249, 2.0, v244, v247
	v_fma_f32 v255, 2.0, v250, v253
	v_sub_f32_e32 v247, v247, v245
	v_sub_f32_e32 v253, v253, v251
	v_fma_f32 v246, -2.0, v244, v246
	v_fma_f32 v252, -2.0, v250, v252
	v_mul_f32_e32 v247, v247, v248
	v_mul_f32_e32 v253, v253, v254
	v_rcp_f32_e32 v247, v247
	v_rcp_f32_e32 v253, v253
	v_mul_f32_e32 v249, v249, v246
	v_mul_f32_e32 v255, v255, v252
	v_fma_f32 v21, v249, v247, v21
	v_fma_f32 v21, v255, v253, v21
	v_mul_f32_e32 v244, v198, v202
	v_mul_f32_e32 v250, v199, v203
	v_mul_f32_e64 v245, -v202, v202
	v_mul_f32_e64 v251, -v203, v203
	v_add_f32_e32 v246, v198, v202
	v_add_f32_e32 v252, v199, v203
	v_fma_f32 v245, -v198, v198, v245
	v_fma_f32 v251, -v199, v199, v251
	v_fma_f32 v247, v10, v246, v11
	v_fma_f32 v253, v10, v252, v11
	v_fma_f32 v246, v13, v210, v14
	v_fma_f32 v252, v13, v211, v14
	v_fma_f32 v248, v12, v206, v245
	v_fma_f32 v254, v12, v207, v251
	v_fma_f32 v249, 2.0, v244, v247
	v_fma_f32 v255, 2.0, v250, v253
	v_sub_f32_e32 v247, v247, v245
	v_sub_f32_e32 v253, v253, v251
	v_fma_f32 v246, -2.0, v244, v246
	v_fma_f32 v252, -2.0, v250, v252
	v_mul_f32_e32 v247, v247, v248
	v_mul_f32_e32 v253, v253, v254
	v_rcp_f32_e32 v247, v247
	v_rcp_f32_e32 v253, v253
	v_mul_f32_e32 v249, v249, v246
	v_mul_f32_e32 v255, v255, v252
	v_fma_f32 v22, v249, v247, v22
	v_fma_f32 v22, v255, v253, v22
	v_mfma_f32_16x16x32_f16 v[196:199], v[24:27], v[168:171], 0
	v_mfma_f32_16x16x32_f16 v[200:203], v[24:27], v[176:179], 0
	v_mfma_f32_16x16x32_f16 v[204:207], v[24:27], v[184:187], v[0:3]
	v_mfma_f32_16x16x32_f16 v[208:211], v[24:27], v[192:195], 0
	s_waitcnt lgkmcnt(0)
	v_cmp_ne_u32_e32 vcc, 0, v9
	s_cbranch_vccnz .Lq_go_3
